# ticket loop back-edges no longer drain outstanding stores before drawing the next ticket (only the loop entry waits)
# speedup vs baseline: 1.0079x; 1.0079x over previous
; __device__ __forceinline__ void attn_conv_phase(const Ptrs& P, const att::AttnArgs& A, int layer, unsigned* qctr, unsigned char* lds, const int wave_) {
;     ...
;     for (;;) {
;         __syncthreads();
;         if (t0_) TK[0] = nxt_;
;         __syncthreads();
;         const int tk = __builtin_amdgcn_readfirstlane(TK[0]);
;         if (tk >= att::N_TICKETS) break;
;         if (t0_) nxt_ = (int)__hip_atomic_fetch_add(qctr, 1u, __ATOMIC_RELAXED, __HIP_MEMORY_SCOPE_AGENT);
.LBB0_439:
	s_and_b64 vcc, exec, s[14:15]
	s_cbranch_vccnz .LBB0_1159
	s_branch .Lticket_top_nowait
